# LN1/router phase: the wave's router weights are fetched in one batch per token group (53 of 128 kept resident in spare registers) instead of an 8-deep load pipeline per product
# speedup vs baseline: 1.0277x; 1.0040x over previous
; #define GAS __attribute__((address_space(1)))
; #define LAS __attribute__((address_space(3)))
; template <bool SKIP_MIX>
; __device__ __forceinline__ void p8_ln_router(Frame& F0, const In& I) {
;     ...
;     LAS float* hs = (LAS float*)(F.lds + P8_HS); LAS float* part = (LAS float*)(F.lds + P8_PART); LAS float* lg = (LAS float*)(F.lds + P8_LOG); LAS int* hist = (LAS int*)(F.lds + P8_HIST);
;     const int lane = F.lane, w = F.wave;
;     if (F.tid < 32) hist[F.tid] = 0;
;     const int kq = lane >> 4, col = lane & 15;
;     float ln_w[32], ln_b[32];
; #pragma unroll
;     for (int j = 0; j < 8; ++j) { const f32x4 a = *(const GAS f32x4*)(I.ln1_w + 4 * lane + 256 * j), b = *(const GAS f32x4*)(I.ln1_b + 4 * lane + 256 * j);
; #pragma unroll
;         for (int e = 0; e < 4; ++e) { ln_w[4 * j + e] = a[e]; ln_b[4 * j + e] = b[e]; } }
;     __syncthreads();
;     if (F.vcu & 1) { __builtin_amdgcn_s_sleep(127); __builtin_amdgcn_s_sleep(127); }
;     const float* zsrc = I.x; const bf16* mixb = (const bf16*)(F.ws + WS_Z);
;     for (int g = F.vcu; g < T / 16; g += F.G) {
;     ...
;         const float* bp = I.w_router + (size_t)(256 * w + 4 * kq) * NE + col;
; #pragma unroll 4
;         for (int kk = 0; kk < 16; ++kk) {
;             const f32x4 a = *(const LAS f32x4*)(ap + 16 * kk);
; #pragma unroll
;             for (int e = 0; e < 4; ++e) {
;                 const float b0 = bp[(size_t)(16 * kk + e) * NE], b1 = bp[(size_t)(16 * kk + e) * NE + 16];
.LBB0_1511:
	v_readlane_b32 s0, v254, 62
	v_readlane_b32 s1, v254, 63
	s_andn2_b64 vcc, exec, s[0:1]
	s_cbranch_vccnz .LBB0_1518
	s_ashr_i32 s12, s4, 6
	v_lshrrev_b32_e32 v70, 2, v74
	v_and_b32_e32 v67, 15, v74
	s_lshl_b32 s0, s12, 10
	v_and_b32_e32 v70, 12, v70
	v_mul_u32_u24_e32 v69, 0x2010, v67
	s_add_i32 s0, s0, 0
	v_lshlrev_b32_e32 v71, 2, v70
	s_lshl_b32 s8, s12, 1
	v_add3_u32 v152, s0, v69, v71
	s_add_i32 s0, 0, 0x20100
	s_add_i32 s1, 0, 0x24100
	s_add_u32 s6, s96, 0x200000
	s_addc_u32 s7, s97, 0
	v_readlane_b32 s36, v254, 37
	v_lshlrev_b32_e32 v69, 2, v67
	v_and_b32_e32 v67, 0x3fffffe0, v74
	v_lshlrev_b32_e32 v71, 2, v74
	s_add_u32 s10, s96, 0x300000
	v_readlane_b32 s37, v254, 38
	v_readlane_b32 s38, v254, 39
	v_readlane_b32 s39, v254, 40
	v_readlane_b32 s40, v254, 41
	v_readlane_b32 s41, v254, 42
	v_readlane_b32 s42, v254, 43
	v_readlane_b32 s43, v254, 44
	v_readlane_b32 s44, v254, 45
	v_readlane_b32 s45, v254, 46
	v_readlane_b32 s46, v254, 47
	v_readlane_b32 s47, v254, 48
	v_readlane_b32 s48, v254, 49
	v_readlane_b32 s49, v254, 50
	v_readlane_b32 s50, v254, 51
	v_readlane_b32 s51, v254, 52
	v_lshlrev_b32_e32 v67, 2, v67
	v_and_b32_e32 v76, 0x7c, v71
	v_add_u32_e32 v154, s1, v71
	s_addc_u32 s11, s97, 0
	s_lshl_b32 s1, s12, 11
	v_mov_b32_e32 v77, 0
	s_mov_b64 s[14:15], s[42:43]
	s_mov_b64 s[16:17], s[44:45]
	v_readlane_b32 s36, v254, 5
	v_add3_u32 v153, s0, v67, v76
	s_add_i32 s1, s1, s0
	v_lshl_add_u64 v[78:79], s[16:17], 0, v[76:77]
	v_mov_b32_e32 v67, v77
	v_readlane_b32 s37, v254, 6
	v_lshlrev_b32_e32 v76, 3, v68
	v_add_u32_e32 v75, 0, v66
	v_add_u32_e32 v73, s1, v69
	v_lshl_add_u64 v[80:81], s[36:37], 0, v[66:67]
	v_lshl_add_u64 v[82:83], s[56:57], 0, v[76:77]
	v_lshl_add_u64 v[66:67], s[96:97], 0, v[76:77]
	s_mov_b64 s[0:1], 0xc0000000
	v_lshlrev_b32_e32 v76, 2, v68
	v_lshl_add_u64 v[84:85], v[66:67], 0, s[0:1]
	v_lshl_add_u64 v[66:67], s[96:97], 0, v[76:77]
	s_mov_b64 s[0:1], 0xd0000000
	v_lshl_add_u64 v[86:87], v[66:67], 0, s[0:1]
	v_lshl_or_b32 v66, s12, 8, v70
	v_ashrrev_i32_e32 v67, 31, v66
	v_lshlrev_b64 v[66:67], 7, v[66:67]
	v_lshlrev_b32_e32 v71, 7, v74
	v_or_b32_e32 v66, v66, v69
	s_or_b32 s13, s8, 1
	v_lshlrev_b32_e32 v72, 7, v70
	v_lshl_add_u64 v[88:89], s[14:15], 0, v[66:67]
	v_add_u32_e32 v66, 0, v71
	v_cmp_gt_i32_e64 s[4:5], 16, v74
	s_mul_i32 s9, s12, 0x4020
	s_mul_i32 s18, s13, 0x2010
	s_movk_i32 s19, 0x1000
	s_mov_b32 s12, 0x3f9837f0
	v_mov_b32_e32 v76, 0x3727c5ac
	s_mov_b32 s20, 0xf800000
	v_mov_b32_e32 v155, 0x260
	v_add_u32_e32 v156, v73, v72
	v_add_u32_e32 v157, 0x24100, v66
	v_mov_b32_e32 v158, 1
	s_add_i32 s21, 0, 0x24900
	v_mov_b32_e32 v159, 0xff7fc99e
	s_mov_b32 s22, s70
	v_readlane_b32 s38, v254, 7
	v_readlane_b32 s39, v254, 8
	v_readlane_b32 s40, v254, 9
	v_readlane_b32 s41, v254, 10
	v_readlane_b32 s42, v254, 11
	v_readlane_b32 s43, v254, 12
	v_readlane_b32 s44, v254, 13
	v_readlane_b32 s45, v254, 14
	v_readlane_b32 s46, v254, 15
	v_readlane_b32 s47, v254, 16
	v_readlane_b32 s48, v254, 17
	v_readlane_b32 s49, v254, 18
	v_readlane_b32 s50, v254, 19
	v_readlane_b32 s51, v254, 20
	s_waitcnt vmcnt(0)
	s_mov_b64 s[0:1], 0x1000
	v_mov_b32_e32 v108, v88
	v_mov_b32_e32 v109, v89
	v_lshl_add_u64 v[108:109], v[108:109], 0, s[0:1]
	v_lshl_add_u64 v[108:109], v[108:109], 0, s[0:1]
	v_lshl_add_u64 v[108:109], v[108:109], 0, s[0:1]
	v_lshl_add_u64 v[108:109], v[108:109], 0, s[0:1]
	global_load_dword v200, v[108:109], off offset:2240
	global_load_dword v201, v[108:109], off offset:2304
	global_load_dword v202, v[108:109], off offset:2368
	global_load_dword v203, v[108:109], off offset:2432
	global_load_dword v204, v[108:109], off offset:2496
	v_lshl_add_u64 v[108:109], v[108:109], 0, s[0:1]
	global_load_dword v205, v[108:109], off offset:0
	global_load_dword v206, v[108:109], off offset:64
	global_load_dword v207, v[108:109], off offset:128
	global_load_dword v208, v[108:109], off offset:192
	global_load_dword v209, v[108:109], off offset:256
	global_load_dword v210, v[108:109], off offset:320
	global_load_dword v211, v[108:109], off offset:384
	global_load_dword v212, v[108:109], off offset:448
	global_load_dword v213, v[108:109], off offset:2048
	global_load_dword v214, v[108:109], off offset:2112
	global_load_dword v215, v[108:109], off offset:2176
	global_load_dword v216, v[108:109], off offset:2240
	global_load_dword v217, v[108:109], off offset:2304
	global_load_dword v218, v[108:109], off offset:2368
	global_load_dword v219, v[108:109], off offset:2432
	global_load_dword v220, v[108:109], off offset:2496
	v_lshl_add_u64 v[108:109], v[108:109], 0, s[0:1]
	global_load_dword v221, v[108:109], off offset:0
	global_load_dword v222, v[108:109], off offset:64
	global_load_dword v223, v[108:109], off offset:128
	global_load_dword v224, v[108:109], off offset:192
	global_load_dword v225, v[108:109], off offset:256
	global_load_dword v226, v[108:109], off offset:320
	global_load_dword v227, v[108:109], off offset:384
	global_load_dword v228, v[108:109], off offset:448
	global_load_dword v229, v[108:109], off offset:2048
	global_load_dword v230, v[108:109], off offset:2112
	global_load_dword v231, v[108:109], off offset:2176
	global_load_dword v232, v[108:109], off offset:2240
	global_load_dword v233, v[108:109], off offset:2304
	global_load_dword v234, v[108:109], off offset:2368
	global_load_dword v235, v[108:109], off offset:2432
	global_load_dword v236, v[108:109], off offset:2496
	v_lshl_add_u64 v[108:109], v[108:109], 0, s[0:1]
	global_load_dword v237, v[108:109], off offset:0
	global_load_dword v238, v[108:109], off offset:64
	global_load_dword v239, v[108:109], off offset:128
	global_load_dword v240, v[108:109], off offset:192
	global_load_dword v241, v[108:109], off offset:256
	global_load_dword v242, v[108:109], off offset:320
	global_load_dword v243, v[108:109], off offset:384
	global_load_dword v244, v[108:109], off offset:448
	global_load_dword v245, v[108:109], off offset:2048
	global_load_dword v246, v[108:109], off offset:2112
	global_load_dword v247, v[108:109], off offset:2176
	global_load_dword v248, v[108:109], off offset:2240
	global_load_dword v249, v[108:109], off offset:2304
	global_load_dword v250, v[108:109], off offset:2368
	global_load_dword v251, v[108:109], off offset:2432
	global_load_dword v252, v[108:109], off offset:2496
	s_waitcnt vmcnt(0)
	s_branch .LBB0_1514

; #define LAS __attribute__((address_space(3)))
; template <bool SKIP_MIX>
; __device__ __forceinline__ void p8_ln_router(Frame& F0, const In& I) {
;     ...
;         f32x4 c0 = (f32x4){0.f, 0.f, 0.f, 0.f}, c1 = c0;
;         const LAS float* ap = hs + col * P8_PITCH + 256 * w + 4 * kq;
;         const float* bp = I.w_router + (size_t)(256 * w + 4 * kq) * NE + col;
; #pragma unroll 4
;         for (int kk = 0; kk < 16; ++kk) {
;             const f32x4 a = *(const LAS f32x4*)(ap + 16 * kk);
; #pragma unroll
;             for (int e = 0; e < 4; ++e) {
;                 const float b0 = bp[(size_t)(16 * kk + e) * NE], b1 = bp[(size_t)(16 * kk + e) * NE + 16];
;                 c0 = __builtin_amdgcn_mfma_f32_16x16x4f32(a[e], b0, c0, 0, 0, 0);
;                 c1 = __builtin_amdgcn_mfma_f32_16x16x4f32(a[e], b1, c1, 0, 0, 0);
;             }
;         }
.LBB0_1515:
	s_waitcnt vmcnt(16)
	s_mov_b64 s[0:1], 0x1000
	v_mov_b32_e32 v108, v88
	v_mov_b32_e32 v109, v89
	global_load_dword v117, v[108:109], off offset:0
	global_load_dword v118, v[108:109], off offset:64
	global_load_dword v119, v[108:109], off offset:128
	global_load_dword v120, v[108:109], off offset:192
	global_load_dword v121, v[108:109], off offset:256
	global_load_dword v122, v[108:109], off offset:320
	global_load_dword v123, v[108:109], off offset:384
	global_load_dword v124, v[108:109], off offset:448
	global_load_dword v125, v[108:109], off offset:2048
	global_load_dword v126, v[108:109], off offset:2112
	global_load_dword v127, v[108:109], off offset:2176
	global_load_dword v128, v[108:109], off offset:2240
	global_load_dword v129, v[108:109], off offset:2304
	global_load_dword v130, v[108:109], off offset:2368
	global_load_dword v131, v[108:109], off offset:2432
	global_load_dword v132, v[108:109], off offset:2496
	v_lshl_add_u64 v[108:109], v[108:109], 0, s[0:1]
	global_load_dword v133, v[108:109], off offset:0
	global_load_dword v134, v[108:109], off offset:64
	global_load_dword v135, v[108:109], off offset:128
	global_load_dword v136, v[108:109], off offset:192
	global_load_dword v137, v[108:109], off offset:256
	global_load_dword v138, v[108:109], off offset:320
	global_load_dword v139, v[108:109], off offset:384
	global_load_dword v140, v[108:109], off offset:448
	global_load_dword v141, v[108:109], off offset:2048
	global_load_dword v142, v[108:109], off offset:2112
	global_load_dword v143, v[108:109], off offset:2176
	global_load_dword v144, v[108:109], off offset:2240
	global_load_dword v145, v[108:109], off offset:2304
	global_load_dword v146, v[108:109], off offset:2368
	global_load_dword v147, v[108:109], off offset:2432
	global_load_dword v148, v[108:109], off offset:2496
	v_lshl_add_u64 v[108:109], v[108:109], 0, s[0:1]
	global_load_dword v149, v[108:109], off offset:0
	global_load_dword v150, v[108:109], off offset:64
	global_load_dword v151, v[108:109], off offset:128
	global_load_dword v160, v[108:109], off offset:192
	global_load_dword v161, v[108:109], off offset:256
	global_load_dword v162, v[108:109], off offset:320
	global_load_dword v163, v[108:109], off offset:384
	global_load_dword v164, v[108:109], off offset:448
	global_load_dword v165, v[108:109], off offset:2048
	global_load_dword v166, v[108:109], off offset:2112
	global_load_dword v167, v[108:109], off offset:2176
	global_load_dword v168, v[108:109], off offset:2240
	ds_read_b128 v[92:95], v90
	ds_read_b128 v[96:99], v90 offset:64
	ds_read_b128 v[100:103], v90 offset:128
	ds_read_b128 v[104:107], v90 offset:192
	s_waitcnt lgkmcnt(3)
	global_load_dword v169, v[108:109], off offset:2304
	s_waitcnt vmcnt(43)
	v_mfma_f32_16x16x4_f32 v[66:69], v92, v117, v[66:69]
	v_mfma_f32_16x16x4_f32 v[70:73], v92, v118, v[70:73]
	global_load_dword v170, v[108:109], off offset:2368
	s_waitcnt vmcnt(42)
	v_mfma_f32_16x16x4_f32 v[66:69], v93, v119, v[66:69]
	v_mfma_f32_16x16x4_f32 v[70:73], v93, v120, v[70:73]
	global_load_dword v171, v[108:109], off offset:2432
	s_waitcnt vmcnt(41)
	v_mfma_f32_16x16x4_f32 v[66:69], v94, v121, v[66:69]
	v_mfma_f32_16x16x4_f32 v[70:73], v94, v122, v[70:73]
	global_load_dword v172, v[108:109], off offset:2496
	s_waitcnt vmcnt(40)
	v_mfma_f32_16x16x4_f32 v[66:69], v95, v123, v[66:69]
	v_mfma_f32_16x16x4_f32 v[70:73], v95, v124, v[70:73]
	s_waitcnt lgkmcnt(2)
	v_lshl_add_u64 v[108:109], v[108:109], 0, s[0:1]
	global_load_dword v173, v[108:109], off offset:0
	s_waitcnt vmcnt(39)
	v_mfma_f32_16x16x4_f32 v[66:69], v96, v125, v[66:69]
	v_mfma_f32_16x16x4_f32 v[70:73], v96, v126, v[70:73]
	global_load_dword v174, v[108:109], off offset:64
	s_waitcnt vmcnt(38)
	v_mfma_f32_16x16x4_f32 v[66:69], v97, v127, v[66:69]
	v_mfma_f32_16x16x4_f32 v[70:73], v97, v128, v[70:73]
	global_load_dword v175, v[108:109], off offset:128
	s_waitcnt vmcnt(37)
	v_mfma_f32_16x16x4_f32 v[66:69], v98, v129, v[66:69]
	v_mfma_f32_16x16x4_f32 v[70:73], v98, v130, v[70:73]
	global_load_dword v176, v[108:109], off offset:192
	s_waitcnt vmcnt(36)
	v_mfma_f32_16x16x4_f32 v[66:69], v99, v131, v[66:69]
	v_mfma_f32_16x16x4_f32 v[70:73], v99, v132, v[70:73]
	s_waitcnt lgkmcnt(1)
	global_load_dword v177, v[108:109], off offset:256
	s_waitcnt vmcnt(35)
	v_mfma_f32_16x16x4_f32 v[66:69], v100, v133, v[66:69]
	v_mfma_f32_16x16x4_f32 v[70:73], v100, v134, v[70:73]
	global_load_dword v178, v[108:109], off offset:320
	s_waitcnt vmcnt(34)
	v_mfma_f32_16x16x4_f32 v[66:69], v101, v135, v[66:69]
	v_mfma_f32_16x16x4_f32 v[70:73], v101, v136, v[70:73]
	global_load_dword v179, v[108:109], off offset:384
	s_waitcnt vmcnt(33)
	v_mfma_f32_16x16x4_f32 v[66:69], v102, v137, v[66:69]
	v_mfma_f32_16x16x4_f32 v[70:73], v102, v138, v[70:73]
	global_load_dword v180, v[108:109], off offset:448
	s_waitcnt vmcnt(32)
	v_mfma_f32_16x16x4_f32 v[66:69], v103, v139, v[66:69]
	v_mfma_f32_16x16x4_f32 v[70:73], v103, v140, v[70:73]
	s_waitcnt lgkmcnt(0)
	global_load_dword v181, v[108:109], off offset:2048
	s_waitcnt vmcnt(31)
	v_mfma_f32_16x16x4_f32 v[66:69], v104, v141, v[66:69]
	v_mfma_f32_16x16x4_f32 v[70:73], v104, v142, v[70:73]
	global_load_dword v182, v[108:109], off offset:2112
	s_waitcnt vmcnt(30)
	v_mfma_f32_16x16x4_f32 v[66:69], v105, v143, v[66:69]
	v_mfma_f32_16x16x4_f32 v[70:73], v105, v144, v[70:73]
	global_load_dword v183, v[108:109], off offset:2176
	s_waitcnt vmcnt(29)
	v_mfma_f32_16x16x4_f32 v[66:69], v106, v145, v[66:69]
	v_mfma_f32_16x16x4_f32 v[70:73], v106, v146, v[70:73]
	global_load_dword v184, v[108:109], off offset:2240
	s_waitcnt vmcnt(28)
; #define LAS __attribute__((address_space(3)))
; template <bool SKIP_MIX>
; __device__ __forceinline__ void p8_ln_router(Frame& F0, const In& I) {
;     ...
;         for (int kk = 0; kk < 16; ++kk) {
;             const f32x4 a = *(const LAS f32x4*)(ap + 16 * kk);
; #pragma unroll
;             for (int e = 0; e < 4; ++e) {
;                 const float b0 = bp[(size_t)(16 * kk + e) * NE], b1 = bp[(size_t)(16 * kk + e) * NE + 16];
;                 c0 = __builtin_amdgcn_mfma_f32_16x16x4f32(a[e], b0, c0, 0, 0, 0);
;                 c1 = __builtin_amdgcn_mfma_f32_16x16x4f32(a[e], b1, c1, 0, 0, 0);
;             }
;         }
	v_mfma_f32_16x16x4_f32 v[66:69], v107, v147, v[66:69]
	v_mfma_f32_16x16x4_f32 v[70:73], v107, v148, v[70:73]
	ds_read_b128 v[92:95], v90 offset:256
	ds_read_b128 v[96:99], v90 offset:320
	ds_read_b128 v[100:103], v90 offset:384
	ds_read_b128 v[104:107], v90 offset:448
	s_waitcnt lgkmcnt(3)
	global_load_dword v185, v[108:109], off offset:2304
	s_waitcnt vmcnt(27)
	v_mfma_f32_16x16x4_f32 v[66:69], v92, v149, v[66:69]
	v_mfma_f32_16x16x4_f32 v[70:73], v92, v150, v[70:73]
	global_load_dword v186, v[108:109], off offset:2368
	s_waitcnt vmcnt(26)
	v_mfma_f32_16x16x4_f32 v[66:69], v93, v151, v[66:69]
	v_mfma_f32_16x16x4_f32 v[70:73], v93, v160, v[70:73]
	global_load_dword v187, v[108:109], off offset:2432
	s_waitcnt vmcnt(25)
	v_mfma_f32_16x16x4_f32 v[66:69], v94, v161, v[66:69]
	v_mfma_f32_16x16x4_f32 v[70:73], v94, v162, v[70:73]
	global_load_dword v188, v[108:109], off offset:2496
	s_waitcnt vmcnt(24)
	v_mfma_f32_16x16x4_f32 v[66:69], v95, v163, v[66:69]
	v_mfma_f32_16x16x4_f32 v[70:73], v95, v164, v[70:73]
	s_waitcnt lgkmcnt(2)
	v_lshl_add_u64 v[108:109], v[108:109], 0, s[0:1]
	global_load_dword v189, v[108:109], off offset:0
	s_waitcnt vmcnt(23)
	v_mfma_f32_16x16x4_f32 v[66:69], v96, v165, v[66:69]
	v_mfma_f32_16x16x4_f32 v[70:73], v96, v166, v[70:73]
	global_load_dword v190, v[108:109], off offset:64
	s_waitcnt vmcnt(22)
	v_mfma_f32_16x16x4_f32 v[66:69], v97, v167, v[66:69]
	v_mfma_f32_16x16x4_f32 v[70:73], v97, v168, v[70:73]
	global_load_dword v191, v[108:109], off offset:128
	s_waitcnt vmcnt(21)
	v_mfma_f32_16x16x4_f32 v[66:69], v98, v169, v[66:69]
	v_mfma_f32_16x16x4_f32 v[70:73], v98, v170, v[70:73]
	global_load_dword v192, v[108:109], off offset:192
	s_waitcnt vmcnt(20)
	v_mfma_f32_16x16x4_f32 v[66:69], v99, v171, v[66:69]
	v_mfma_f32_16x16x4_f32 v[70:73], v99, v172, v[70:73]
	s_waitcnt lgkmcnt(1)
	global_load_dword v193, v[108:109], off offset:256
	s_waitcnt vmcnt(19)
	v_mfma_f32_16x16x4_f32 v[66:69], v100, v173, v[66:69]
	v_mfma_f32_16x16x4_f32 v[70:73], v100, v174, v[70:73]
	global_load_dword v194, v[108:109], off offset:320
	s_waitcnt vmcnt(18)
	v_mfma_f32_16x16x4_f32 v[66:69], v101, v175, v[66:69]
	v_mfma_f32_16x16x4_f32 v[70:73], v101, v176, v[70:73]
	global_load_dword v195, v[108:109], off offset:384
	s_waitcnt vmcnt(17)
	v_mfma_f32_16x16x4_f32 v[66:69], v102, v177, v[66:69]
	v_mfma_f32_16x16x4_f32 v[70:73], v102, v178, v[70:73]
	global_load_dword v196, v[108:109], off offset:448
	s_waitcnt vmcnt(16)
	v_mfma_f32_16x16x4_f32 v[66:69], v103, v179, v[66:69]
	v_mfma_f32_16x16x4_f32 v[70:73], v103, v180, v[70:73]
	s_waitcnt lgkmcnt(0)
	global_load_dword v197, v[108:109], off offset:2048
	s_waitcnt vmcnt(15)
	v_mfma_f32_16x16x4_f32 v[66:69], v104, v181, v[66:69]
	v_mfma_f32_16x16x4_f32 v[70:73], v104, v182, v[70:73]
	global_load_dword v198, v[108:109], off offset:2112
	s_waitcnt vmcnt(14)
	v_mfma_f32_16x16x4_f32 v[66:69], v105, v183, v[66:69]
	v_mfma_f32_16x16x4_f32 v[70:73], v105, v184, v[70:73]
	global_load_dword v199, v[108:109], off offset:2176
	s_waitcnt vmcnt(13)
	v_mfma_f32_16x16x4_f32 v[66:69], v106, v185, v[66:69]
	v_mfma_f32_16x16x4_f32 v[70:73], v106, v186, v[70:73]
	s_waitcnt vmcnt(11)
	v_mfma_f32_16x16x4_f32 v[66:69], v107, v187, v[66:69]
	v_mfma_f32_16x16x4_f32 v[70:73], v107, v188, v[70:73]
	ds_read_b128 v[92:95], v90 offset:512
	ds_read_b128 v[96:99], v90 offset:576
	ds_read_b128 v[100:103], v90 offset:640
	ds_read_b128 v[104:107], v90 offset:704
	s_waitcnt lgkmcnt(3)
	s_waitcnt vmcnt(9)
	v_mfma_f32_16x16x4_f32 v[66:69], v92, v189, v[66:69]
	v_mfma_f32_16x16x4_f32 v[70:73], v92, v190, v[70:73]
	s_waitcnt vmcnt(7)
	v_mfma_f32_16x16x4_f32 v[66:69], v93, v191, v[66:69]
	v_mfma_f32_16x16x4_f32 v[70:73], v93, v192, v[70:73]
	s_waitcnt vmcnt(5)
	v_mfma_f32_16x16x4_f32 v[66:69], v94, v193, v[66:69]
	v_mfma_f32_16x16x4_f32 v[70:73], v94, v194, v[70:73]
	s_waitcnt vmcnt(3)
	v_mfma_f32_16x16x4_f32 v[66:69], v95, v195, v[66:69]
	v_mfma_f32_16x16x4_f32 v[70:73], v95, v196, v[70:73]
	s_waitcnt lgkmcnt(2)
	s_waitcnt vmcnt(1)
	v_mfma_f32_16x16x4_f32 v[66:69], v96, v197, v[66:69]
	v_mfma_f32_16x16x4_f32 v[70:73], v96, v198, v[70:73]
	s_waitcnt vmcnt(0)
	v_mfma_f32_16x16x4_f32 v[66:69], v97, v199, v[66:69]
	v_mfma_f32_16x16x4_f32 v[70:73], v97, v200, v[70:73]
	v_mfma_f32_16x16x4_f32 v[66:69], v98, v201, v[66:69]
	v_mfma_f32_16x16x4_f32 v[70:73], v98, v202, v[70:73]
	v_mfma_f32_16x16x4_f32 v[66:69], v99, v203, v[66:69]
	v_mfma_f32_16x16x4_f32 v[70:73], v99, v204, v[70:73]
	s_waitcnt lgkmcnt(1)
	v_mfma_f32_16x16x4_f32 v[66:69], v100, v205, v[66:69]
	v_mfma_f32_16x16x4_f32 v[70:73], v100, v206, v[70:73]
	v_mfma_f32_16x16x4_f32 v[66:69], v101, v207, v[66:69]
	v_mfma_f32_16x16x4_f32 v[70:73], v101, v208, v[70:73]
	v_mfma_f32_16x16x4_f32 v[66:69], v102, v209, v[66:69]
	v_mfma_f32_16x16x4_f32 v[70:73], v102, v210, v[70:73]
	v_mfma_f32_16x16x4_f32 v[66:69], v103, v211, v[66:69]
	v_mfma_f32_16x16x4_f32 v[70:73], v103, v212, v[70:73]
	s_waitcnt lgkmcnt(0)
	v_mfma_f32_16x16x4_f32 v[66:69], v104, v213, v[66:69]
	v_mfma_f32_16x16x4_f32 v[70:73], v104, v214, v[70:73]
	v_mfma_f32_16x16x4_f32 v[66:69], v105, v215, v[66:69]
	v_mfma_f32_16x16x4_f32 v[70:73], v105, v216, v[70:73]
	v_mfma_f32_16x16x4_f32 v[66:69], v106, v217, v[66:69]
	v_mfma_f32_16x16x4_f32 v[70:73], v106, v218, v[70:73]
	v_mfma_f32_16x16x4_f32 v[66:69], v107, v219, v[66:69]
	v_mfma_f32_16x16x4_f32 v[70:73], v107, v220, v[70:73]
	ds_read_b128 v[92:95], v90 offset:768
	ds_read_b128 v[96:99], v90 offset:832
	ds_read_b128 v[100:103], v90 offset:896
	ds_read_b128 v[104:107], v90 offset:960
	s_waitcnt lgkmcnt(3)
; #define LAS __attribute__((address_space(3)))
; template <bool SKIP_MIX>
; __device__ __forceinline__ void p8_ln_router(Frame& F0, const In& I) {
;     ...
;         for (int kk = 0; kk < 16; ++kk) {
;             const f32x4 a = *(const LAS f32x4*)(ap + 16 * kk);
; #pragma unroll
;             for (int e = 0; e < 4; ++e) {
;                 const float b0 = bp[(size_t)(16 * kk + e) * NE], b1 = bp[(size_t)(16 * kk + e) * NE + 16];
;                 c0 = __builtin_amdgcn_mfma_f32_16x16x4f32(a[e], b0, c0, 0, 0, 0);
;                 c1 = __builtin_amdgcn_mfma_f32_16x16x4f32(a[e], b1, c1, 0, 0, 0);
;             }
;         }
; #pragma unroll
;         for (int i = 0; i < 4; ++i) { part[(w * 16 + 4 * kq + i) * 32 + col] = c0[i]; part[(w * 16 + 4 * kq + i) * 32 + 16 + col] = c1[i]; }
;         __syncthreads();
;         { const int tl = F.tid >> 5, e = F.tid & 31; float s = I.b_router[e];
; #pragma unroll
;             for (int ww = 0; ww < 8; ++ww) s += part[(ww * 16 + tl) * 32 + e];
;             lg[tl * 32 + e] = s; }
;         __syncthreads();
;         if (F.tid < 16) {
;             const int tl = F.tid; float lv[32];
; #pragma unroll
;             for (int e = 0; e < 32; ++e) lv[e] = lg[tl * 32 + e];
;             int ti[4]; float tv[4];
; #pragma unroll
;             for (int k = 0; k < 4; ++k) { float best = -3.4e38f; int bi = 0;
; #pragma unroll
;                 for (int e = 0; e < 32; ++e) { const bool tk = lv[e] > best; best = tk ? lv[e] : best; bi = tk ? e : bi; }
	v_mfma_f32_16x16x4_f32 v[66:69], v92, v221, v[66:69]
	v_mfma_f32_16x16x4_f32 v[70:73], v92, v222, v[70:73]
	v_mfma_f32_16x16x4_f32 v[66:69], v93, v223, v[66:69]
	v_mfma_f32_16x16x4_f32 v[70:73], v93, v224, v[70:73]
	v_mfma_f32_16x16x4_f32 v[66:69], v94, v225, v[66:69]
	v_mfma_f32_16x16x4_f32 v[70:73], v94, v226, v[70:73]
	v_mfma_f32_16x16x4_f32 v[66:69], v95, v227, v[66:69]
	v_mfma_f32_16x16x4_f32 v[70:73], v95, v228, v[70:73]
	s_waitcnt lgkmcnt(2)
	v_mfma_f32_16x16x4_f32 v[66:69], v96, v229, v[66:69]
	v_mfma_f32_16x16x4_f32 v[70:73], v96, v230, v[70:73]
	v_mfma_f32_16x16x4_f32 v[66:69], v97, v231, v[66:69]
	v_mfma_f32_16x16x4_f32 v[70:73], v97, v232, v[70:73]
	v_mfma_f32_16x16x4_f32 v[66:69], v98, v233, v[66:69]
	v_mfma_f32_16x16x4_f32 v[70:73], v98, v234, v[70:73]
	v_mfma_f32_16x16x4_f32 v[66:69], v99, v235, v[66:69]
	v_mfma_f32_16x16x4_f32 v[70:73], v99, v236, v[70:73]
	s_waitcnt lgkmcnt(1)
	v_mfma_f32_16x16x4_f32 v[66:69], v100, v237, v[66:69]
	v_mfma_f32_16x16x4_f32 v[70:73], v100, v238, v[70:73]
	v_mfma_f32_16x16x4_f32 v[66:69], v101, v239, v[66:69]
	v_mfma_f32_16x16x4_f32 v[70:73], v101, v240, v[70:73]
	v_mfma_f32_16x16x4_f32 v[66:69], v102, v241, v[66:69]
	v_mfma_f32_16x16x4_f32 v[70:73], v102, v242, v[70:73]
	v_mfma_f32_16x16x4_f32 v[66:69], v103, v243, v[66:69]
	v_mfma_f32_16x16x4_f32 v[70:73], v103, v244, v[70:73]
	s_waitcnt lgkmcnt(0)
	v_mfma_f32_16x16x4_f32 v[66:69], v104, v245, v[66:69]
	v_mfma_f32_16x16x4_f32 v[70:73], v104, v246, v[70:73]
	v_mfma_f32_16x16x4_f32 v[66:69], v105, v247, v[66:69]
	v_mfma_f32_16x16x4_f32 v[70:73], v105, v248, v[70:73]
	v_mfma_f32_16x16x4_f32 v[66:69], v106, v249, v[66:69]
	v_mfma_f32_16x16x4_f32 v[70:73], v106, v250, v[70:73]
	v_mfma_f32_16x16x4_f32 v[66:69], v107, v251, v[66:69]
	v_mfma_f32_16x16x4_f32 v[70:73], v107, v252, v[70:73]
	s_nop 8
	ds_write2_b32 v156, v66, v70 offset1:16
	ds_write2_b32 v156, v67, v71 offset0:32 offset1:48
	ds_write2_b32 v156, v68, v72 offset0:64 offset1:80
	ds_write2_b32 v156, v69, v73 offset0:96 offset1:112
	s_waitcnt lgkmcnt(0)
	s_barrier
	global_load_dword v90, v[78:79], off
	ds_read2st64_b32 v[66:67], v153 offset1:8
	ds_read2st64_b32 v[68:69], v153 offset0:16 offset1:24
	ds_read2st64_b32 v[70:71], v153 offset0:32 offset1:40
	ds_read2st64_b32 v[72:73], v153 offset0:48 offset1:56
	s_waitcnt vmcnt(0) lgkmcnt(3)
	v_add_f32_e32 v66, v90, v66
	v_add_f32_e32 v66, v66, v67
	s_waitcnt lgkmcnt(2)
	v_add_f32_e32 v66, v66, v68
	v_add_f32_e32 v66, v66, v69
	s_waitcnt lgkmcnt(1)
	v_add_f32_e32 v66, v66, v70
	v_add_f32_e32 v66, v66, v71
	s_waitcnt lgkmcnt(0)
	v_add_f32_e32 v66, v66, v72
	v_add_f32_e32 v66, v66, v73
	ds_write_b32 v154, v66
	s_waitcnt lgkmcnt(0)
	s_barrier
	s_and_saveexec_b64 s[0:1], s[4:5]
	s_cbranch_execz .LBB0_1513
	ds_read_b128 v[68:71], v157
	ds_read_b128 v[90:93], v157 offset:16
	ds_read_b128 v[94:97], v157 offset:32
	ds_read_b128 v[98:101], v157 offset:48
	ds_read_b128 v[102:105], v157 offset:64
	ds_read_b128 v[106:109], v157 offset:80
	ds_read_b128 v[110:113], v157 offset:96
	ds_read_b128 v[114:117], v157 offset:112
	s_waitcnt lgkmcnt(7)
	v_max_f32_e32 v66, v68, v68
	v_max_f32_e32 v66, 0xff7fc99e, v66
	v_cmp_gt_f32_e32 vcc, v69, v66
	s_nop 1
	v_cndmask_b32_e32 v66, v66, v69, vcc
	v_cndmask_b32_e64 v67, 0, 1, vcc
	v_cmp_gt_f32_e32 vcc, v70, v66
	s_nop 1
	v_cndmask_b32_e32 v66, v66, v70, vcc
	v_cndmask_b32_e64 v67, v67, 2, vcc
	v_cmp_gt_f32_e32 vcc, v71, v66
	s_nop 1
	v_cndmask_b32_e32 v66, v66, v71, vcc
	v_cndmask_b32_e64 v67, v67, 3, vcc
	s_waitcnt lgkmcnt(6)
	v_cmp_gt_f32_e32 vcc, v90, v66
	s_nop 1
	v_cndmask_b32_e32 v66, v66, v90, vcc
	v_cndmask_b32_e64 v67, v67, 4, vcc
	v_cmp_gt_f32_e32 vcc, v91, v66
	s_nop 1
	v_cndmask_b32_e32 v66, v66, v91, vcc
	v_cndmask_b32_e64 v67, v67, 5, vcc
	v_cmp_gt_f32_e32 vcc, v92, v66
	s_nop 1
	v_cndmask_b32_e32 v66, v66, v92, vcc
	v_cndmask_b32_e64 v67, v67, 6, vcc
	v_cmp_gt_f32_e32 vcc, v93, v66
	s_nop 1
	v_cndmask_b32_e32 v66, v66, v93, vcc
	v_cndmask_b32_e64 v67, v67, 7, vcc
	s_waitcnt lgkmcnt(5)
	v_cmp_gt_f32_e32 vcc, v94, v66
	s_nop 1
	v_cndmask_b32_e32 v66, v66, v94, vcc
	v_cndmask_b32_e64 v67, v67, 8, vcc
	v_cmp_gt_f32_e32 vcc, v95, v66
	s_nop 1
	v_cndmask_b32_e32 v66, v66, v95, vcc
	v_cndmask_b32_e64 v67, v67, 9, vcc
	v_cmp_gt_f32_e32 vcc, v96, v66
	s_nop 1
	v_cndmask_b32_e32 v66, v66, v96, vcc
	v_cndmask_b32_e64 v67, v67, 10, vcc
	v_cmp_gt_f32_e32 vcc, v97, v66
	s_nop 1
	v_cndmask_b32_e32 v66, v66, v97, vcc
	v_cndmask_b32_e64 v67, v67, 11, vcc
	s_waitcnt lgkmcnt(4)
	v_cmp_gt_f32_e32 vcc, v98, v66
	s_nop 1
	v_cndmask_b32_e32 v66, v66, v98, vcc
	v_cndmask_b32_e64 v67, v67, 12, vcc
	v_cmp_gt_f32_e32 vcc, v99, v66
	s_nop 1
	v_cndmask_b32_e32 v66, v66, v99, vcc
	v_cndmask_b32_e64 v67, v67, 13, vcc
	v_cmp_gt_f32_e32 vcc, v100, v66
	s_nop 1
	v_cndmask_b32_e32 v66, v66, v100, vcc
	v_cndmask_b32_e64 v67, v67, 14, vcc
	v_cmp_gt_f32_e32 vcc, v101, v66
	s_nop 1
	v_cndmask_b32_e32 v66, v66, v101, vcc
	v_cndmask_b32_e64 v67, v67, 15, vcc
	s_waitcnt lgkmcnt(3)
	v_cmp_gt_f32_e32 vcc, v102, v66
	s_nop 1
	v_cndmask_b32_e32 v66, v66, v102, vcc
	v_cndmask_b32_e64 v67, v67, 16, vcc
	v_cmp_gt_f32_e32 vcc, v103, v66
	s_nop 1
	v_cndmask_b32_e32 v66, v66, v103, vcc
	v_cndmask_b32_e64 v67, v67, 17, vcc
	v_cmp_gt_f32_e32 vcc, v104, v66
	s_nop 1
	v_cndmask_b32_e32 v66, v66, v104, vcc
	v_cndmask_b32_e64 v67, v67, 18, vcc
	v_cmp_gt_f32_e32 vcc, v105, v66
	s_nop 1
	v_cndmask_b32_e32 v66, v66, v105, vcc
	v_cndmask_b32_e64 v67, v67, 19, vcc
	s_waitcnt lgkmcnt(2)
; template <bool SKIP_MIX>
; __device__ __forceinline__ void p8_ln_router(Frame& F0, const In& I) {
;     ...
;         if (F.tid < 16) {
;             const int tl = F.tid; float lv[32];
; #pragma unroll
;             for (int e = 0; e < 32; ++e) lv[e] = lg[tl * 32 + e];
;             int ti[4]; float tv[4];
; #pragma unroll
;             for (int k = 0; k < 4; ++k) { float best = -3.4e38f; int bi = 0;
; #pragma unroll
;                 for (int e = 0; e < 32; ++e) { const bool tk = lv[e] > best; best = tk ? lv[e] : best; bi = tk ? e : bi; }
;                 ti[k] = bi; tv[k] = best;
; #pragma unroll
;                 for (int e = 0; e < 32; ++e) lv[e] = (e == bi) ? -3.4e38f : lv[e]; }
	v_cmp_gt_f32_e32 vcc, v106, v66
	s_nop 1
	v_cndmask_b32_e32 v66, v66, v106, vcc
	v_cndmask_b32_e64 v67, v67, 20, vcc
	v_cmp_gt_f32_e32 vcc, v107, v66
	s_nop 1
	v_cndmask_b32_e32 v66, v66, v107, vcc
	v_cndmask_b32_e64 v67, v67, 21, vcc
	v_cmp_gt_f32_e32 vcc, v108, v66
	s_nop 1
	v_cndmask_b32_e32 v66, v66, v108, vcc
	v_cndmask_b32_e64 v67, v67, 22, vcc
	v_cmp_gt_f32_e32 vcc, v109, v66
	s_nop 1
	v_cndmask_b32_e32 v66, v66, v109, vcc
	v_cndmask_b32_e64 v67, v67, 23, vcc
	s_waitcnt lgkmcnt(1)
	v_cmp_gt_f32_e32 vcc, v110, v66
	s_nop 1
	v_cndmask_b32_e32 v66, v66, v110, vcc
	v_cndmask_b32_e64 v67, v67, 24, vcc
	v_cmp_gt_f32_e32 vcc, v111, v66
	s_nop 1
	v_cndmask_b32_e32 v66, v66, v111, vcc
	v_cndmask_b32_e64 v67, v67, 25, vcc
	v_cmp_gt_f32_e32 vcc, v112, v66
	s_nop 1
	v_cndmask_b32_e32 v66, v66, v112, vcc
	v_cndmask_b32_e64 v67, v67, 26, vcc
	v_cmp_gt_f32_e32 vcc, v113, v66
	s_nop 1
	v_cndmask_b32_e32 v66, v66, v113, vcc
	v_cndmask_b32_e64 v67, v67, 27, vcc
	s_waitcnt lgkmcnt(0)
	v_cmp_gt_f32_e32 vcc, v114, v66
	s_nop 1
	v_cndmask_b32_e32 v66, v66, v114, vcc
	v_cndmask_b32_e64 v67, v67, 28, vcc
	v_cmp_gt_f32_e32 vcc, v115, v66
	s_nop 1
	v_cndmask_b32_e32 v66, v66, v115, vcc
	v_cndmask_b32_e64 v67, v67, 29, vcc
	v_cmp_gt_f32_e32 vcc, v116, v66
	s_nop 1
	v_cndmask_b32_e32 v72, v66, v116, vcc
	v_cndmask_b32_e64 v67, v67, 30, vcc
	v_cmp_gt_f32_e32 vcc, v117, v72
	s_nop 1
	v_cndmask_b32_e64 v66, v67, 31, vcc
	v_cndmask_b32_e32 v73, v72, v117, vcc
	v_cmp_ne_u32_e32 vcc, 0, v66
	s_nop 1
	v_cndmask_b32_e32 v68, v159, v68, vcc
	v_cmp_ne_u32_e32 vcc, 1, v66
	v_max_f32_e32 v67, v68, v68
	v_max_f32_e32 v67, 0xff7fc99e, v67
	v_cndmask_b32_e32 v69, v159, v69, vcc
	v_cmp_ne_u32_e32 vcc, 2, v66
	s_nop 1
	v_cndmask_b32_e32 v70, v159, v70, vcc
	v_cmp_ne_u32_e32 vcc, 3, v66
	s_nop 1
	v_cndmask_b32_e32 v71, v159, v71, vcc
	v_cmp_ne_u32_e32 vcc, 4, v66
	s_nop 1
	v_cndmask_b32_e32 v72, v159, v90, vcc
	v_cmp_ne_u32_e32 vcc, 5, v66
	s_nop 1
	v_cndmask_b32_e32 v90, v159, v91, vcc
	v_cmp_ne_u32_e32 vcc, 6, v66
	s_nop 1
	v_cndmask_b32_e32 v91, v159, v92, vcc
	v_cmp_ne_u32_e32 vcc, 7, v66
	s_nop 1
	v_cndmask_b32_e32 v92, v159, v93, vcc
	v_cmp_ne_u32_e32 vcc, 8, v66
	s_nop 1
	v_cndmask_b32_e32 v93, v159, v94, vcc
	v_cmp_ne_u32_e32 vcc, 9, v66
	s_nop 1
	v_cndmask_b32_e32 v94, v159, v95, vcc
	v_cmp_ne_u32_e32 vcc, 10, v66
	s_nop 1
	v_cndmask_b32_e32 v95, v159, v96, vcc
	v_cmp_ne_u32_e32 vcc, 11, v66
	s_nop 1
	v_cndmask_b32_e32 v96, v159, v97, vcc
	v_cmp_ne_u32_e32 vcc, 12, v66
	s_nop 1
	v_cndmask_b32_e32 v97, v159, v98, vcc
	v_cmp_ne_u32_e32 vcc, 13, v66
	s_nop 1
	v_cndmask_b32_e32 v98, v159, v99, vcc
	v_cmp_ne_u32_e32 vcc, 14, v66
	s_nop 1
	v_cndmask_b32_e32 v99, v159, v100, vcc
	v_cmp_ne_u32_e32 vcc, 15, v66
	s_nop 1
	v_cndmask_b32_e32 v100, v159, v101, vcc
	v_cmp_ne_u32_e32 vcc, 16, v66
	s_nop 1
	v_cndmask_b32_e32 v101, v159, v102, vcc
	v_cmp_ne_u32_e32 vcc, 17, v66
	s_nop 1
	v_cndmask_b32_e32 v102, v159, v103, vcc
	v_cmp_ne_u32_e32 vcc, 18, v66
	s_nop 1
	v_cndmask_b32_e32 v103, v159, v104, vcc
	v_cmp_ne_u32_e32 vcc, 19, v66
	s_nop 1
	v_cndmask_b32_e32 v104, v159, v105, vcc
	v_cmp_ne_u32_e32 vcc, 20, v66
	s_nop 1
	v_cndmask_b32_e32 v105, v159, v106, vcc
	v_cmp_ne_u32_e32 vcc, 21, v66
	s_nop 1
	v_cndmask_b32_e32 v106, v159, v107, vcc
	v_cmp_ne_u32_e32 vcc, 22, v66
	s_nop 1
	v_cndmask_b32_e32 v107, v159, v108, vcc
	v_cmp_ne_u32_e32 vcc, 23, v66
	s_nop 1
	v_cndmask_b32_e32 v108, v159, v109, vcc
	v_cmp_ne_u32_e32 vcc, 24, v66
	s_nop 1
	v_cndmask_b32_e32 v109, v159, v110, vcc
	v_cmp_ne_u32_e32 vcc, 25, v66
	s_nop 1
	v_cndmask_b32_e32 v110, v159, v111, vcc
	v_cmp_ne_u32_e32 vcc, 26, v66
	s_nop 1
	v_cndmask_b32_e32 v111, v159, v112, vcc
	v_cmp_ne_u32_e32 vcc, 27, v66
	s_nop 1
	v_cndmask_b32_e32 v112, v159, v113, vcc
	v_cmp_ne_u32_e32 vcc, 28, v66
	s_nop 1
	v_cndmask_b32_e32 v113, v159, v114, vcc
	v_cmp_ne_u32_e32 vcc, 29, v66
	s_nop 1
	v_cndmask_b32_e32 v114, v159, v115, vcc
	v_cmp_ne_u32_e32 vcc, 30, v66
	s_nop 1
	v_cndmask_b32_e32 v115, v159, v116, vcc
	v_cmp_ne_u32_e32 vcc, 31, v66
	s_nop 1
	v_cndmask_b32_e32 v116, v159, v117, vcc
	v_cmp_gt_f32_e32 vcc, v69, v67
	s_nop 1
	v_cndmask_b32_e32 v67, v67, v69, vcc
	v_cndmask_b32_e64 v117, 0, 1, vcc
	v_cmp_gt_f32_e32 vcc, v70, v67
	s_nop 1
	v_cndmask_b32_e32 v67, v67, v70, vcc
	v_cndmask_b32_e64 v117, v117, 2, vcc
	v_cmp_gt_f32_e32 vcc, v71, v67
	s_nop 1
	v_cndmask_b32_e32 v67, v67, v71, vcc
	v_cndmask_b32_e64 v117, v117, 3, vcc
	v_cmp_gt_f32_e32 vcc, v72, v67
	s_nop 1
	v_cndmask_b32_e32 v67, v67, v72, vcc
	v_cndmask_b32_e64 v117, v117, 4, vcc
	v_cmp_gt_f32_e32 vcc, v90, v67
	s_nop 1
	v_cndmask_b32_e32 v67, v67, v90, vcc
	v_cndmask_b32_e64 v117, v117, 5, vcc
	v_cmp_gt_f32_e32 vcc, v91, v67
	s_nop 1
	v_cndmask_b32_e32 v67, v67, v91, vcc
	v_cndmask_b32_e64 v117, v117, 6, vcc
	v_cmp_gt_f32_e32 vcc, v92, v67
	s_nop 1
	v_cndmask_b32_e32 v67, v67, v92, vcc
	v_cndmask_b32_e64 v117, v117, 7, vcc
	v_cmp_gt_f32_e32 vcc, v93, v67
	s_nop 1
	v_cndmask_b32_e32 v67, v67, v93, vcc
	v_cndmask_b32_e64 v117, v117, 8, vcc
	v_cmp_gt_f32_e32 vcc, v94, v67
	s_nop 1
	v_cndmask_b32_e32 v67, v67, v94, vcc
	v_cndmask_b32_e64 v117, v117, 9, vcc
	v_cmp_gt_f32_e32 vcc, v95, v67
	s_nop 1
	v_cndmask_b32_e32 v67, v67, v95, vcc
	v_cndmask_b32_e64 v117, v117, 10, vcc
	v_cmp_gt_f32_e32 vcc, v96, v67
	s_nop 1
	v_cndmask_b32_e32 v67, v67, v96, vcc
	v_cndmask_b32_e64 v117, v117, 11, vcc
	v_cmp_gt_f32_e32 vcc, v97, v67
	s_nop 1
	v_cndmask_b32_e32 v67, v67, v97, vcc
	v_cndmask_b32_e64 v117, v117, 12, vcc
	v_cmp_gt_f32_e32 vcc, v98, v67
	s_nop 1
	v_cndmask_b32_e32 v67, v67, v98, vcc
	v_cndmask_b32_e64 v117, v117, 13, vcc
	v_cmp_gt_f32_e32 vcc, v99, v67
	s_nop 1
; template <bool SKIP_MIX>
; __device__ __forceinline__ void p8_ln_router(Frame& F0, const In& I) {
;     ...
;             for (int k = 0; k < 4; ++k) { float best = -3.4e38f; int bi = 0;
; #pragma unroll
;                 for (int e = 0; e < 32; ++e) { const bool tk = lv[e] > best; best = tk ? lv[e] : best; bi = tk ? e : bi; }
;                 ti[k] = bi; tv[k] = best;
; #pragma unroll
;                 for (int e = 0; e < 32; ++e) lv[e] = (e == bi) ? -3.4e38f : lv[e]; }
	v_cndmask_b32_e32 v67, v67, v99, vcc
	v_cndmask_b32_e64 v117, v117, 14, vcc
	v_cmp_gt_f32_e32 vcc, v100, v67
	s_nop 1
	v_cndmask_b32_e32 v67, v67, v100, vcc
	v_cndmask_b32_e64 v117, v117, 15, vcc
	v_cmp_gt_f32_e32 vcc, v101, v67
	s_nop 1
	v_cndmask_b32_e32 v67, v67, v101, vcc
	v_cndmask_b32_e64 v117, v117, 16, vcc
	v_cmp_gt_f32_e32 vcc, v102, v67
	s_nop 1
	v_cndmask_b32_e32 v67, v67, v102, vcc
	v_cndmask_b32_e64 v117, v117, 17, vcc
	v_cmp_gt_f32_e32 vcc, v103, v67
	s_nop 1
	v_cndmask_b32_e32 v67, v67, v103, vcc
	v_cndmask_b32_e64 v117, v117, 18, vcc
	v_cmp_gt_f32_e32 vcc, v104, v67
	s_nop 1
	v_cndmask_b32_e32 v67, v67, v104, vcc
	v_cndmask_b32_e64 v117, v117, 19, vcc
	v_cmp_gt_f32_e32 vcc, v105, v67
	s_nop 1
	v_cndmask_b32_e32 v67, v67, v105, vcc
	v_cndmask_b32_e64 v117, v117, 20, vcc
	v_cmp_gt_f32_e32 vcc, v106, v67
	s_nop 1
	v_cndmask_b32_e32 v67, v67, v106, vcc
	v_cndmask_b32_e64 v117, v117, 21, vcc
	v_cmp_gt_f32_e32 vcc, v107, v67
	s_nop 1
	v_cndmask_b32_e32 v67, v67, v107, vcc
	v_cndmask_b32_e64 v117, v117, 22, vcc
	v_cmp_gt_f32_e32 vcc, v108, v67
	s_nop 1
	v_cndmask_b32_e32 v67, v67, v108, vcc
	v_cndmask_b32_e64 v117, v117, 23, vcc
	v_cmp_gt_f32_e32 vcc, v109, v67
	s_nop 1
	v_cndmask_b32_e32 v67, v67, v109, vcc
	v_cndmask_b32_e64 v117, v117, 24, vcc
	v_cmp_gt_f32_e32 vcc, v110, v67
	s_nop 1
	v_cndmask_b32_e32 v67, v67, v110, vcc
	v_cndmask_b32_e64 v117, v117, 25, vcc
	v_cmp_gt_f32_e32 vcc, v111, v67
	s_nop 1
	v_cndmask_b32_e32 v67, v67, v111, vcc
	v_cndmask_b32_e64 v117, v117, 26, vcc
	v_cmp_gt_f32_e32 vcc, v112, v67
	s_nop 1
	v_cndmask_b32_e32 v67, v67, v112, vcc
	v_cndmask_b32_e64 v117, v117, 27, vcc
	v_cmp_gt_f32_e32 vcc, v113, v67
	s_nop 1
	v_cndmask_b32_e32 v67, v67, v113, vcc
	v_cndmask_b32_e64 v117, v117, 28, vcc
	v_cmp_gt_f32_e32 vcc, v114, v67
	s_nop 1
	v_cndmask_b32_e32 v67, v67, v114, vcc
	v_cndmask_b32_e64 v117, v117, 29, vcc
	v_cmp_gt_f32_e32 vcc, v115, v67
	s_nop 1
	v_cndmask_b32_e32 v118, v67, v115, vcc
	v_cndmask_b32_e64 v117, v117, 30, vcc
	v_cmp_gt_f32_e32 vcc, v116, v118
	s_nop 1
	v_cndmask_b32_e64 v67, v117, 31, vcc
	v_cndmask_b32_e32 v117, v118, v116, vcc
	v_cmp_ne_u32_e32 vcc, 0, v67
	s_nop 1
	v_cndmask_b32_e32 v118, v159, v68, vcc
	v_cmp_ne_u32_e32 vcc, 1, v67
	v_max_f32_e32 v68, v118, v118
	v_max_f32_e32 v68, 0xff7fc99e, v68
	v_cndmask_b32_e32 v69, v159, v69, vcc
	v_cmp_ne_u32_e32 vcc, 2, v67
	s_nop 1
	v_cndmask_b32_e32 v70, v159, v70, vcc
	v_cmp_ne_u32_e32 vcc, 3, v67
	s_nop 1
	v_cndmask_b32_e32 v71, v159, v71, vcc
	v_cmp_ne_u32_e32 vcc, 4, v67
	s_nop 1
	v_cndmask_b32_e32 v72, v159, v72, vcc
	v_cmp_ne_u32_e32 vcc, 5, v67
	s_nop 1
	v_cndmask_b32_e32 v90, v159, v90, vcc
	v_cmp_ne_u32_e32 vcc, 6, v67
	s_nop 1
	v_cndmask_b32_e32 v91, v159, v91, vcc
	v_cmp_ne_u32_e32 vcc, 7, v67
	s_nop 1
	v_cndmask_b32_e32 v92, v159, v92, vcc
	v_cmp_ne_u32_e32 vcc, 8, v67
	s_nop 1
	v_cndmask_b32_e32 v93, v159, v93, vcc
	v_cmp_ne_u32_e32 vcc, 9, v67
	s_nop 1
	v_cndmask_b32_e32 v94, v159, v94, vcc
	v_cmp_ne_u32_e32 vcc, 10, v67
	s_nop 1
	v_cndmask_b32_e32 v95, v159, v95, vcc
	v_cmp_ne_u32_e32 vcc, 11, v67
	s_nop 1
	v_cndmask_b32_e32 v96, v159, v96, vcc
	v_cmp_ne_u32_e32 vcc, 12, v67
	s_nop 1
	v_cndmask_b32_e32 v97, v159, v97, vcc
	v_cmp_ne_u32_e32 vcc, 13, v67
	s_nop 1
	v_cndmask_b32_e32 v98, v159, v98, vcc
	v_cmp_ne_u32_e32 vcc, 14, v67
	s_nop 1
	v_cndmask_b32_e32 v99, v159, v99, vcc
	v_cmp_ne_u32_e32 vcc, 15, v67
	s_nop 1
	v_cndmask_b32_e32 v100, v159, v100, vcc
	v_cmp_ne_u32_e32 vcc, 16, v67
	s_nop 1
	v_cndmask_b32_e32 v101, v159, v101, vcc
	v_cmp_ne_u32_e32 vcc, 17, v67
	s_nop 1
	v_cndmask_b32_e32 v102, v159, v102, vcc
	v_cmp_ne_u32_e32 vcc, 18, v67
	s_nop 1
	v_cndmask_b32_e32 v103, v159, v103, vcc
	v_cmp_ne_u32_e32 vcc, 19, v67
	s_nop 1
	v_cndmask_b32_e32 v104, v159, v104, vcc
	v_cmp_ne_u32_e32 vcc, 20, v67
	s_nop 1
	v_cndmask_b32_e32 v105, v159, v105, vcc
	v_cmp_ne_u32_e32 vcc, 21, v67
	s_nop 1
	v_cndmask_b32_e32 v106, v159, v106, vcc
	v_cmp_ne_u32_e32 vcc, 22, v67
	s_nop 1
	v_cndmask_b32_e32 v107, v159, v107, vcc
	v_cmp_ne_u32_e32 vcc, 23, v67
	s_nop 1
	v_cndmask_b32_e32 v108, v159, v108, vcc
	v_cmp_ne_u32_e32 vcc, 24, v67
	s_nop 1
	v_cndmask_b32_e32 v109, v159, v109, vcc
	v_cmp_ne_u32_e32 vcc, 25, v67
	s_nop 1
	v_cndmask_b32_e32 v110, v159, v110, vcc
	v_cmp_ne_u32_e32 vcc, 26, v67
	s_nop 1
	v_cndmask_b32_e32 v111, v159, v111, vcc
	v_cmp_ne_u32_e32 vcc, 27, v67
	s_nop 1
	v_cndmask_b32_e32 v112, v159, v112, vcc
	v_cmp_ne_u32_e32 vcc, 28, v67
	s_nop 1
	v_cndmask_b32_e32 v113, v159, v113, vcc
	v_cmp_ne_u32_e32 vcc, 29, v67
	s_nop 1
	v_cndmask_b32_e32 v114, v159, v114, vcc
	v_cmp_ne_u32_e32 vcc, 30, v67
	s_nop 1
	v_cndmask_b32_e32 v115, v159, v115, vcc
	v_cmp_ne_u32_e32 vcc, 31, v67
	s_nop 1
	v_cndmask_b32_e32 v116, v159, v116, vcc
	v_cmp_gt_f32_e32 vcc, v69, v68
	s_nop 1
	v_cndmask_b32_e32 v68, v68, v69, vcc
	v_cndmask_b32_e64 v119, 0, 1, vcc
	v_cmp_gt_f32_e32 vcc, v70, v68
	s_nop 1
	v_cndmask_b32_e32 v68, v68, v70, vcc
	v_cndmask_b32_e64 v119, v119, 2, vcc
	v_cmp_gt_f32_e32 vcc, v71, v68
	s_nop 1
	v_cndmask_b32_e32 v68, v68, v71, vcc
	v_cndmask_b32_e64 v119, v119, 3, vcc
	v_cmp_gt_f32_e32 vcc, v72, v68
	s_nop 1
	v_cndmask_b32_e32 v68, v68, v72, vcc
	v_cndmask_b32_e64 v119, v119, 4, vcc
	v_cmp_gt_f32_e32 vcc, v90, v68
	s_nop 1
	v_cndmask_b32_e32 v68, v68, v90, vcc
	v_cndmask_b32_e64 v119, v119, 5, vcc
	v_cmp_gt_f32_e32 vcc, v91, v68
	s_nop 1
	v_cndmask_b32_e32 v68, v68, v91, vcc
	v_cndmask_b32_e64 v119, v119, 6, vcc
	v_cmp_gt_f32_e32 vcc, v92, v68
	s_nop 1
	v_cndmask_b32_e32 v68, v68, v92, vcc
	v_cndmask_b32_e64 v119, v119, 7, vcc
	v_cmp_gt_f32_e32 vcc, v93, v68
	s_nop 1
	v_cndmask_b32_e32 v68, v68, v93, vcc
; template <bool SKIP_MIX>
; __device__ __forceinline__ void p8_ln_router(Frame& F0, const In& I) {
;     ...
;             for (int k = 0; k < 4; ++k) { float best = -3.4e38f; int bi = 0;
; #pragma unroll
;                 for (int e = 0; e < 32; ++e) { const bool tk = lv[e] > best; best = tk ? lv[e] : best; bi = tk ? e : bi; }
;                 ti[k] = bi; tv[k] = best;
; #pragma unroll
;                 for (int e = 0; e < 32; ++e) lv[e] = (e == bi) ? -3.4e38f : lv[e]; }
	v_cndmask_b32_e64 v119, v119, 8, vcc
	v_cmp_gt_f32_e32 vcc, v94, v68
	s_nop 1
	v_cndmask_b32_e32 v68, v68, v94, vcc
	v_cndmask_b32_e64 v119, v119, 9, vcc
	v_cmp_gt_f32_e32 vcc, v95, v68
	s_nop 1
	v_cndmask_b32_e32 v68, v68, v95, vcc
	v_cndmask_b32_e64 v119, v119, 10, vcc
	v_cmp_gt_f32_e32 vcc, v96, v68
	s_nop 1
	v_cndmask_b32_e32 v68, v68, v96, vcc
	v_cndmask_b32_e64 v119, v119, 11, vcc
	v_cmp_gt_f32_e32 vcc, v97, v68
	s_nop 1
	v_cndmask_b32_e32 v68, v68, v97, vcc
	v_cndmask_b32_e64 v119, v119, 12, vcc
	v_cmp_gt_f32_e32 vcc, v98, v68
	s_nop 1
	v_cndmask_b32_e32 v68, v68, v98, vcc
	v_cndmask_b32_e64 v119, v119, 13, vcc
	v_cmp_gt_f32_e32 vcc, v99, v68
	s_nop 1
	v_cndmask_b32_e32 v68, v68, v99, vcc
	v_cndmask_b32_e64 v119, v119, 14, vcc
	v_cmp_gt_f32_e32 vcc, v100, v68
	s_nop 1
	v_cndmask_b32_e32 v68, v68, v100, vcc
	v_cndmask_b32_e64 v119, v119, 15, vcc
	v_cmp_gt_f32_e32 vcc, v101, v68
	s_nop 1
	v_cndmask_b32_e32 v68, v68, v101, vcc
	v_cndmask_b32_e64 v119, v119, 16, vcc
	v_cmp_gt_f32_e32 vcc, v102, v68
	s_nop 1
	v_cndmask_b32_e32 v68, v68, v102, vcc
	v_cndmask_b32_e64 v119, v119, 17, vcc
	v_cmp_gt_f32_e32 vcc, v103, v68
	s_nop 1
	v_cndmask_b32_e32 v68, v68, v103, vcc
	v_cndmask_b32_e64 v119, v119, 18, vcc
	v_cmp_gt_f32_e32 vcc, v104, v68
	s_nop 1
	v_cndmask_b32_e32 v68, v68, v104, vcc
	v_cndmask_b32_e64 v119, v119, 19, vcc
	v_cmp_gt_f32_e32 vcc, v105, v68
	s_nop 1
	v_cndmask_b32_e32 v68, v68, v105, vcc
	v_cndmask_b32_e64 v119, v119, 20, vcc
	v_cmp_gt_f32_e32 vcc, v106, v68
	s_nop 1
	v_cndmask_b32_e32 v68, v68, v106, vcc
	v_cndmask_b32_e64 v119, v119, 21, vcc
	v_cmp_gt_f32_e32 vcc, v107, v68
	s_nop 1
	v_cndmask_b32_e32 v68, v68, v107, vcc
	v_cndmask_b32_e64 v119, v119, 22, vcc
	v_cmp_gt_f32_e32 vcc, v108, v68
	s_nop 1
	v_cndmask_b32_e32 v68, v68, v108, vcc
	v_cndmask_b32_e64 v119, v119, 23, vcc
	v_cmp_gt_f32_e32 vcc, v109, v68
	s_nop 1
	v_cndmask_b32_e32 v68, v68, v109, vcc
	v_cndmask_b32_e64 v119, v119, 24, vcc
	v_cmp_gt_f32_e32 vcc, v110, v68
	s_nop 1
	v_cndmask_b32_e32 v68, v68, v110, vcc
	v_cndmask_b32_e64 v119, v119, 25, vcc
	v_cmp_gt_f32_e32 vcc, v111, v68
	s_nop 1
	v_cndmask_b32_e32 v68, v68, v111, vcc
	v_cndmask_b32_e64 v119, v119, 26, vcc
	v_cmp_gt_f32_e32 vcc, v112, v68
	s_nop 1
	v_cndmask_b32_e32 v68, v68, v112, vcc
	v_cndmask_b32_e64 v119, v119, 27, vcc
	v_cmp_gt_f32_e32 vcc, v113, v68
	s_nop 1
	v_cndmask_b32_e32 v68, v68, v113, vcc
	v_cndmask_b32_e64 v119, v119, 28, vcc
	v_cmp_gt_f32_e32 vcc, v114, v68
	s_nop 1
	v_cndmask_b32_e32 v68, v68, v114, vcc
	v_cndmask_b32_e64 v119, v119, 29, vcc
	v_cmp_gt_f32_e32 vcc, v115, v68
	s_nop 1
	v_cndmask_b32_e32 v120, v68, v115, vcc
	v_cndmask_b32_e64 v119, v119, 30, vcc
	v_cmp_gt_f32_e32 vcc, v116, v120
	s_nop 1
	v_cndmask_b32_e64 v68, v119, 31, vcc
	v_cndmask_b32_e32 v119, v120, v116, vcc
	v_cmp_ne_u32_e32 vcc, 0, v68
	s_nop 1
	v_cndmask_b32_e32 v118, v159, v118, vcc
	v_cmp_ne_u32_e32 vcc, 1, v68
	v_max_f32_e32 v118, v118, v118
	v_max_f32_e32 v118, 0xff7fc99e, v118
	v_cndmask_b32_e32 v69, v159, v69, vcc
	v_cmp_ne_u32_e32 vcc, 2, v68
	s_nop 1
	v_cndmask_b32_e32 v70, v159, v70, vcc
	v_cmp_ne_u32_e32 vcc, 3, v68
	s_nop 1
	v_cndmask_b32_e32 v71, v159, v71, vcc
	v_cmp_ne_u32_e32 vcc, 4, v68
	s_nop 1
	v_cndmask_b32_e32 v72, v159, v72, vcc
	v_cmp_ne_u32_e32 vcc, 5, v68
	s_nop 1
	v_cndmask_b32_e32 v90, v159, v90, vcc
	v_cmp_ne_u32_e32 vcc, 6, v68
	s_nop 1
	v_cndmask_b32_e32 v91, v159, v91, vcc
	v_cmp_ne_u32_e32 vcc, 7, v68
	s_nop 1
	v_cndmask_b32_e32 v92, v159, v92, vcc
	v_cmp_ne_u32_e32 vcc, 8, v68
	s_nop 1
	v_cndmask_b32_e32 v93, v159, v93, vcc
	v_cmp_ne_u32_e32 vcc, 9, v68
	s_nop 1
	v_cndmask_b32_e32 v94, v159, v94, vcc
	v_cmp_ne_u32_e32 vcc, 10, v68
	s_nop 1
	v_cndmask_b32_e32 v95, v159, v95, vcc
	v_cmp_ne_u32_e32 vcc, 11, v68
	s_nop 1
	v_cndmask_b32_e32 v96, v159, v96, vcc
	v_cmp_ne_u32_e32 vcc, 12, v68
	s_nop 1
	v_cndmask_b32_e32 v97, v159, v97, vcc
	v_cmp_ne_u32_e32 vcc, 13, v68
	s_nop 1
	v_cndmask_b32_e32 v98, v159, v98, vcc
	v_cmp_ne_u32_e32 vcc, 14, v68
	s_nop 1
	v_cndmask_b32_e32 v99, v159, v99, vcc
	v_cmp_ne_u32_e32 vcc, 15, v68
	s_nop 1
	v_cndmask_b32_e32 v100, v159, v100, vcc
	v_cmp_ne_u32_e32 vcc, 16, v68
	s_nop 1
	v_cndmask_b32_e32 v101, v159, v101, vcc
	v_cmp_ne_u32_e32 vcc, 17, v68
	s_nop 1
	v_cndmask_b32_e32 v102, v159, v102, vcc
	v_cmp_ne_u32_e32 vcc, 18, v68
	s_nop 1
	v_cndmask_b32_e32 v103, v159, v103, vcc
	v_cmp_ne_u32_e32 vcc, 19, v68
	s_nop 1
	v_cndmask_b32_e32 v104, v159, v104, vcc
	v_cmp_ne_u32_e32 vcc, 20, v68
	s_nop 1
	v_cndmask_b32_e32 v105, v159, v105, vcc
	v_cmp_ne_u32_e32 vcc, 21, v68
	s_nop 1
	v_cndmask_b32_e32 v106, v159, v106, vcc
	v_cmp_ne_u32_e32 vcc, 22, v68
	s_nop 1
	v_cndmask_b32_e32 v107, v159, v107, vcc
	v_cmp_ne_u32_e32 vcc, 23, v68
	s_nop 1
	v_cndmask_b32_e32 v108, v159, v108, vcc
	v_cmp_ne_u32_e32 vcc, 24, v68
	s_nop 1
	v_cndmask_b32_e32 v109, v159, v109, vcc
	v_cmp_ne_u32_e32 vcc, 25, v68
	s_nop 1
	v_cndmask_b32_e32 v110, v159, v110, vcc
	v_cmp_ne_u32_e32 vcc, 26, v68
	s_nop 1
	v_cndmask_b32_e32 v111, v159, v111, vcc
	v_cmp_ne_u32_e32 vcc, 27, v68
	s_nop 1
	v_cndmask_b32_e32 v112, v159, v112, vcc
	v_cmp_ne_u32_e32 vcc, 28, v68
	s_nop 1
	v_cndmask_b32_e32 v113, v159, v113, vcc
	v_cmp_ne_u32_e32 vcc, 29, v68
	s_nop 1
	v_cndmask_b32_e32 v114, v159, v114, vcc
	v_cmp_ne_u32_e32 vcc, 30, v68
; #define GAS __attribute__((address_space(1)))
; template <bool SKIP_MIX>
; __device__ __forceinline__ void p8_ln_router(Frame& F0, const In& I) {
;     ...
;             for (int k = 0; k < 4; ++k) { float best = -3.4e38f; int bi = 0;
; #pragma unroll
;                 for (int e = 0; e < 32; ++e) { const bool tk = lv[e] > best; best = tk ? lv[e] : best; bi = tk ? e : bi; }
;                 ti[k] = bi; tv[k] = best;
; #pragma unroll
;                 for (int e = 0; e < 32; ++e) lv[e] = (e == bi) ? -3.4e38f : lv[e]; }
;             float ex[4], sum = 0.f;
; #pragma unroll
;             for (int k = 0; k < 4; ++k) { ex[k] = __expf(tv[k] - tv[0]); sum += ex[k]; }
;             const float inv = 1.f / sum;
;             *(GAS v4u*)((int*)(F.ws + WS_TOPI) + (size_t)(tok0 + tl) * 4) = (v4u){(unsigned)ti[0], (unsigned)ti[1], (unsigned)ti[2], (unsigned)ti[3]};
;             *(GAS f32x4*)((float*)(F.ws + WS_GATE) + (size_t)(tok0 + tl) * 4) = (f32x4){ex[0] * inv, ex[1] * inv, ex[2] * inv, ex[3] * inv};
; #pragma unroll
;             for (int k = 0; k < 4; ++k) __hip_atomic_fetch_add(&hist[ti[k]], 1, __ATOMIC_RELAXED, __HIP_MEMORY_SCOPE_WORKGROUP);
	s_nop 1
	v_cndmask_b32_e32 v115, v159, v115, vcc
	v_cmp_ne_u32_e32 vcc, 31, v68
	s_nop 1
	v_cndmask_b32_e32 v116, v159, v116, vcc
	v_cmp_gt_f32_e32 vcc, v69, v118
	s_nop 1
	v_cndmask_b32_e32 v69, v118, v69, vcc
	v_cndmask_b32_e64 v120, 0, 1, vcc
	v_cmp_gt_f32_e32 vcc, v70, v69
	s_nop 1
	v_cndmask_b32_e32 v69, v69, v70, vcc
	v_cndmask_b32_e64 v118, v120, 2, vcc
	v_cmp_gt_f32_e32 vcc, v71, v69
	s_nop 1
	v_cndmask_b32_e32 v69, v69, v71, vcc
	v_cndmask_b32_e64 v70, v118, 3, vcc
	v_cmp_gt_f32_e32 vcc, v72, v69
	s_nop 1
	v_cndmask_b32_e32 v69, v69, v72, vcc
	v_cndmask_b32_e64 v70, v70, 4, vcc
	v_cmp_gt_f32_e32 vcc, v90, v69
	v_sub_f32_e32 v72, v119, v73
	v_mul_f32_e32 v72, 0x3fb8aa3b, v72
	v_cndmask_b32_e32 v69, v69, v90, vcc
	v_cndmask_b32_e64 v70, v70, 5, vcc
	v_cmp_gt_f32_e32 vcc, v91, v69
	v_exp_f32_e32 v72, v72
	s_nop 0
	v_cndmask_b32_e32 v69, v69, v91, vcc
	v_cndmask_b32_e64 v70, v70, 6, vcc
	v_cmp_gt_f32_e32 vcc, v92, v69
	s_nop 1
	v_cndmask_b32_e32 v69, v69, v92, vcc
	v_cndmask_b32_e64 v70, v70, 7, vcc
	v_cmp_gt_f32_e32 vcc, v93, v69
	s_nop 1
	v_cndmask_b32_e32 v69, v69, v93, vcc
	v_cndmask_b32_e64 v70, v70, 8, vcc
	v_cmp_gt_f32_e32 vcc, v94, v69
	s_nop 1
	v_cndmask_b32_e32 v69, v69, v94, vcc
	v_cndmask_b32_e64 v70, v70, 9, vcc
	v_cmp_gt_f32_e32 vcc, v95, v69
	s_nop 1
	v_cndmask_b32_e32 v69, v69, v95, vcc
	v_cndmask_b32_e64 v70, v70, 10, vcc
	v_cmp_gt_f32_e32 vcc, v96, v69
	s_nop 1
	v_cndmask_b32_e32 v69, v69, v96, vcc
	v_cndmask_b32_e64 v70, v70, 11, vcc
	v_cmp_gt_f32_e32 vcc, v97, v69
	s_nop 1
	v_cndmask_b32_e32 v69, v69, v97, vcc
	v_cndmask_b32_e64 v70, v70, 12, vcc
	v_cmp_gt_f32_e32 vcc, v98, v69
	s_nop 1
	v_cndmask_b32_e32 v69, v69, v98, vcc
	v_cndmask_b32_e64 v70, v70, 13, vcc
	v_cmp_gt_f32_e32 vcc, v99, v69
	s_nop 1
	v_cndmask_b32_e32 v69, v69, v99, vcc
	v_cndmask_b32_e64 v70, v70, 14, vcc
	v_cmp_gt_f32_e32 vcc, v100, v69
	s_nop 1
	v_cndmask_b32_e32 v69, v69, v100, vcc
	v_cndmask_b32_e64 v70, v70, 15, vcc
	v_cmp_gt_f32_e32 vcc, v101, v69
	s_nop 1
	v_cndmask_b32_e32 v69, v69, v101, vcc
	v_cndmask_b32_e64 v70, v70, 16, vcc
	v_cmp_gt_f32_e32 vcc, v102, v69
	s_nop 1
	v_cndmask_b32_e32 v69, v69, v102, vcc
	v_cndmask_b32_e64 v70, v70, 17, vcc
	v_cmp_gt_f32_e32 vcc, v103, v69
	s_nop 1
	v_cndmask_b32_e32 v69, v69, v103, vcc
	v_cndmask_b32_e64 v70, v70, 18, vcc
	v_cmp_gt_f32_e32 vcc, v104, v69
	s_nop 1
	v_cndmask_b32_e32 v69, v69, v104, vcc
	v_cndmask_b32_e64 v70, v70, 19, vcc
	v_cmp_gt_f32_e32 vcc, v105, v69
	s_nop 1
	v_cndmask_b32_e32 v69, v69, v105, vcc
	v_cndmask_b32_e64 v70, v70, 20, vcc
	v_cmp_gt_f32_e32 vcc, v106, v69
	s_nop 1
	v_cndmask_b32_e32 v69, v69, v106, vcc
	v_cndmask_b32_e64 v70, v70, 21, vcc
	v_cmp_gt_f32_e32 vcc, v107, v69
	s_nop 1
	v_cndmask_b32_e32 v69, v69, v107, vcc
	v_cndmask_b32_e64 v70, v70, 22, vcc
	v_cmp_gt_f32_e32 vcc, v108, v69
	s_nop 1
	v_cndmask_b32_e32 v69, v69, v108, vcc
	v_cndmask_b32_e64 v70, v70, 23, vcc
	v_cmp_gt_f32_e32 vcc, v109, v69
	s_nop 1
	v_cndmask_b32_e32 v69, v69, v109, vcc
	v_cndmask_b32_e64 v70, v70, 24, vcc
	v_cmp_gt_f32_e32 vcc, v110, v69
	s_nop 1
	v_cndmask_b32_e32 v69, v69, v110, vcc
	v_cndmask_b32_e64 v70, v70, 25, vcc
	v_cmp_gt_f32_e32 vcc, v111, v69
	s_nop 1
	v_cndmask_b32_e32 v69, v69, v111, vcc
	v_cndmask_b32_e64 v70, v70, 26, vcc
	v_cmp_gt_f32_e32 vcc, v112, v69
	s_nop 1
	v_cndmask_b32_e32 v69, v69, v112, vcc
	v_cndmask_b32_e64 v70, v70, 27, vcc
	v_cmp_gt_f32_e32 vcc, v113, v69
	s_nop 1
	v_cndmask_b32_e32 v69, v69, v113, vcc
	v_cndmask_b32_e64 v70, v70, 28, vcc
	v_cmp_gt_f32_e32 vcc, v114, v69
	s_nop 1
	v_cndmask_b32_e32 v69, v69, v114, vcc
	v_cndmask_b32_e64 v70, v70, 29, vcc
	v_cmp_gt_f32_e32 vcc, v115, v69
	s_nop 1
	v_cndmask_b32_e32 v71, v69, v115, vcc
	v_cndmask_b32_e64 v70, v70, 30, vcc
	v_cmp_gt_f32_e32 vcc, v116, v71
	s_nop 1
	v_cndmask_b32_e64 v69, v70, 31, vcc
	v_sub_f32_e32 v70, v73, v73
	v_cndmask_b32_e32 v90, v71, v116, vcc
	v_mul_f32_e32 v70, 0x3fb8aa3b, v70
	v_sub_f32_e32 v71, v117, v73
	v_exp_f32_e32 v70, v70
	v_mul_f32_e32 v71, 0x3fb8aa3b, v71
	v_exp_f32_e32 v71, v71
	v_sub_f32_e32 v73, v90, v73
	v_mul_f32_e32 v73, 0x3fb8aa3b, v73
	v_exp_f32_e32 v73, v73
	v_add_f32_e32 v90, 0, v70
	v_add_f32_e32 v90, v90, v71
	v_add_f32_e32 v90, v90, v72
	v_add_f32_e32 v90, v90, v73
	v_div_scale_f32 v91, s[14:15], v90, v90, 1.0
	v_rcp_f32_e32 v92, v91
	s_nop 0
	v_fma_f32 v93, -v91, v92, 1.0
	v_fmac_f32_e32 v92, v93, v92
	v_div_scale_f32 v93, vcc, 1.0, v90, 1.0
	v_mul_f32_e32 v94, v93, v92
	v_fma_f32 v95, -v91, v94, v93
	v_fmac_f32_e32 v94, v95, v92
	v_fma_f32 v91, -v91, v94, v93
	v_div_fmas_f32 v91, v91, v92, v94
	v_add_u32_e32 v92, s23, v74
	v_ashrrev_i32_e32 v93, 31, v92
	v_div_fixup_f32 v90, v91, v90, 1.0
	v_lshlrev_b64 v[92:93], 4, v[92:93]
	v_lshl_add_u64 v[94:95], s[6:7], 0, v[92:93]
	v_pk_mul_f32 v[72:73], v[72:73], v[90:91] op_sel_hi:[1,0]
	v_pk_mul_f32 v[70:71], v[70:71], v[90:91] op_sel_hi:[1,0]
	v_lshl_add_u64 v[90:91], s[10:11], 0, v[92:93]
	global_store_dwordx4 v[94:95], v[66:69], off
	global_store_dwordx4 v[90:91], v[70:73], off
	s_nop 0
	v_lshl_add_u32 v66, v66, 2, s21
	ds_add_u32 v66, v158
	v_lshl_add_u32 v66, v67, 2, s21
	ds_add_u32 v66, v158
	v_lshl_add_u32 v66, v68, 2, s21
	ds_add_u32 v66, v158
	v_lshl_add_u32 v66, v69, 2, s21
	ds_add_u32 v66, v158
	s_branch .LBB0_1513
